# baseline (speedup 1.0000x reference)
.LBB1_15:
	s_cmp_gt_i32 s77, 7
	s_cselect_b64 s[52:53], -1, 0
	s_lshl_b32 s4, s77, 2
	s_add_i32 s78, s4, s66
	s_or_b32 s37, s4, s62
	s_lshr_b32 s4, s27, 8
	s_and_b32 s4, s4, 0x7ff8
	v_and_b32_e32 v147, 64, v198
	s_add_i32 s10, s4, s78
	s_lshr_b32 s4, s27, 6
	v_xor_b32_e32 v146, 16, v198
	v_add_u32_e32 v206, 64, v147
	s_and_b32 s4, s4, 0x7fe0
	v_cmp_lt_i32_e32 vcc, v146, v206
	s_add_i32 s54, s4, s37
	s_cmp_lt_i32 s77, 8
	v_cndmask_b32_e32 v146, v198, v146, vcc
	v_lshlrev_b32_e32 v201, 2, v146
	v_mul_f32_e32 v146, v127, v127
	v_mul_f32_e32 v147, v129, v129
	s_cselect_b64 s[6:7], -1, 0
	v_fmac_f32_e32 v146, v126, v126
	v_fmac_f32_e32 v147, v128, v128
	s_and_b64 s[4:5], s[6:7], exec
	v_add_f32_e32 v153, v146, v147
	v_pk_mul_f32 v[146:147], v[124:125], v[124:125]
	v_pk_mul_f32 v[148:149], v[122:123], v[122:123]
	s_cselect_b32 s9, s23, s25
	s_cselect_b32 s8, s22, s24
	v_and_b32_e32 v152, 0x7cf, v199
	v_mov_b32_e32 v150, v146
	v_mov_b32_e32 v151, v148
	v_mov_b32_e32 v148, v147
	global_load_dwordx4 v[138:141], v194, s[8:9] offset:16
	global_load_dwordx4 v[142:145], v194, s[8:9]
	global_load_dwordx4 v[130:133], v194, s[8:9] offset:144
	global_load_dwordx4 v[134:137], v194, s[8:9] offset:128
	v_pk_add_f32 v[146:147], v[150:151], v[148:149]
	v_lshlrev_b32_e32 v170, 7, v152
	v_add_f32_e32 v147, v153, v147
	v_lshl_add_u64 v[158:159], v[172:173], 0, v[170:171]
	v_lshl_add_u64 v[150:151], v[174:175], 0, v[170:171]
	v_add_f32_e32 v207, v146, v147
	global_load_dwordx4 v[146:149], v[150:151], off offset:16
	s_nop 0
	global_load_dwordx4 v[150:153], v[150:151], off
	s_nop 0
	global_load_dwordx4 v[154:157], v[158:159], off offset:16
	s_nop 0
	global_load_dwordx4 v[158:161], v[158:159], off
	v_pk_mul_f32 v[184:185], v[112:113], v[112:113]
	v_pk_mul_f32 v[202:203], v[110:111], v[110:111]
	v_mov_b32_e32 v204, v184
	v_mov_b32_e32 v205, v202
	v_mov_b32_e32 v202, v185
	v_pk_add_f32 v[184:185], v[204:205], v[202:203]
	v_pk_mul_f32 v[202:203], v[106:107], v[106:107]
	v_add_f32_e32 v170, v207, v185
	v_add_f32_e32 v170, v184, v170
	v_pk_mul_f32 v[184:185], v[108:109], v[108:109]
	v_mov_b32_e32 v205, v202
	v_mov_b32_e32 v204, v184
	v_mov_b32_e32 v202, v185
	v_pk_add_f32 v[184:185], v[204:205], v[202:203]
	v_cndmask_b32_e64 v200, 1.0, v197, s[6:7]
	v_add_f32_e32 v170, v185, v170
	v_add_f32_e32 v170, v184, v170
	ds_bpermute_b32 v184, v201, v170
	v_xor_b32_e32 v185, 32, v198
	v_cmp_lt_i32_e32 vcc, v185, v206
	s_cselect_b32 s55, s17, s19
	v_or_b32_e32 v229, 16, v199
	v_cndmask_b32_e32 v185, v198, v185, vcc
	v_lshlrev_b32_e32 v202, 2, v185
	s_waitcnt lgkmcnt(0)
	v_add_f32_e32 v170, v170, v184
	ds_bpermute_b32 v184, v202, v170
	s_waitcnt lgkmcnt(0)
	v_add_f32_e32 v170, v170, v184
	v_fmamk_f32 v170, v170, 0x3c800000, v195
	v_rsq_f32_e32 v244, v170
	s_nop 0
	v_mul_f32_e32 v245, v170, v244
	v_fma_f32 v245, -v245, v244, 1.0
	v_mul_f32_e32 v246, 0.5, v244
	v_fmac_f32_e32 v244, v245, v246
	v_mul_f32_e32 v170, v200, v244
	v_lshl_or_b32 v203, s10, 17, v187
	v_lshl_or_b32 v185, s54, 17, v188
	s_cselect_b32 s54, s16, s18
	s_cselect_b32 s10, s72, 0x1000
	v_pk_mul_f32 v[216:217], v[106:107], v[170:171] op_sel_hi:[1,0]
	v_pk_mul_f32 v[210:211], v[122:123], v[170:171] op_sel_hi:[1,0]
	s_waitcnt vmcnt(0)
	v_pk_mul_f32 v[216:217], v[130:131], v[216:217]
	v_pk_mul_f32 v[210:211], v[138:139], v[210:211]
	v_pk_mul_f32 v[224:225], v[146:147], v[216:217]
	v_pk_mul_f32 v[212:213], v[110:111], v[170:171] op_sel_hi:[1,0]
	v_pk_fma_f32 v[224:225], v[154:155], v[210:211], v[224:225] neg_lo:[0,0,1] neg_hi:[0,0,1]
	v_pk_mul_f32 v[154:155], v[154:155], v[216:217]
	v_pk_mul_f32 v[214:215], v[112:113], v[170:171] op_sel_hi:[1,0]
	v_pk_mul_f32 v[218:219], v[108:109], v[170:171] op_sel_hi:[1,0]
	v_pk_fma_f32 v[154:155], v[146:147], v[210:211], v[154:155]
	v_lshlrev_b32_e32 v146, 6, v199
	v_pk_mul_f32 v[204:205], v[128:129], v[170:171] op_sel_hi:[1,0]
	v_pk_mul_f32 v[206:207], v[126:127], v[170:171] op_sel_hi:[1,0]
	v_pk_mul_f32 v[208:209], v[124:125], v[170:171] op_sel_hi:[1,0]
	v_pk_mul_f32 v[214:215], v[136:137], v[214:215]
	v_pk_mul_f32 v[212:213], v[134:135], v[212:213]
	v_pk_mul_f32 v[218:219], v[132:133], v[218:219]
	v_cndmask_b32_e64 v184, v203, v185, s[6:7]
	v_and_b32_e32 v228, 0x1f000, v146
	v_pk_mul_f32 v[206:207], v[142:143], v[206:207]
	v_pk_mul_f32 v[204:205], v[144:145], v[204:205]
	v_pk_mul_f32 v[208:209], v[140:141], v[208:209]
	v_pk_mul_f32 v[220:221], v[150:151], v[212:213]
	v_pk_mul_f32 v[222:223], v[152:153], v[214:215]
	v_pk_mul_f32 v[226:227], v[148:149], v[218:219]
	v_or3_b32 v146, v228, v189, v184
	v_pk_fma_f32 v[222:223], v[160:161], v[204:205], v[222:223] neg_lo:[0,0,1] neg_hi:[0,0,1]
	v_pk_fma_f32 v[220:221], v[158:159], v[206:207], v[220:221] neg_lo:[0,0,1] neg_hi:[0,0,1]
	v_pk_fma_f32 v[226:227], v[156:157], v[208:209], v[226:227] neg_lo:[0,0,1] neg_hi:[0,0,1]
	v_pk_mul_f32 v[158:159], v[158:159], v[212:213]
	v_pk_mul_f32 v[160:161], v[160:161], v[214:215]
	v_pk_mul_f32 v[156:157], v[156:157], v[218:219]
	v_ashrrev_i32_e32 v147, 31, v146
	v_pk_fma_f32 v[152:153], v[152:153], v[204:205], v[160:161]
	v_pk_fma_f32 v[150:151], v[150:151], v[206:207], v[158:159]
	v_pk_fma_f32 v[156:157], v[148:149], v[208:209], v[156:157]
	v_lshl_add_u64 v[158:159], v[146:147], 1, s[54:55]
	v_cvt_pk_f16_f32 v146, v220, v221
	v_cvt_pk_f16_f32 v147, v222, v223
	v_cvt_pk_f16_f32 v148, v224, v225
	v_cvt_pk_f16_f32 v149, v226, v227
	v_cvt_pk_f16_f32 v150, v150, v151
	v_cvt_pk_f16_f32 v151, v152, v153
	v_cvt_pk_f16_f32 v152, v154, v155
	v_cvt_pk_f16_f32 v153, v156, v157
	global_store_dwordx4 v[158:159], v[146:149], off sc1
	v_pk_mul_f32 v[204:205], v[96:97], v[96:97]
	v_pk_mul_f32 v[206:207], v[94:95], v[94:95]
	v_lshl_add_u64 v[146:147], v[158:159], 0, s[10:11]
	global_store_dwordx4 v[146:147], v[150:153], off sc1
	v_mul_f32_e32 v146, v119, v119
	v_mul_f32_e32 v147, v121, v121
	v_fmac_f32_e32 v146, v118, v118
	v_fmac_f32_e32 v147, v120, v120
	v_add_f32_e32 v153, v146, v147
	v_pk_mul_f32 v[146:147], v[116:117], v[116:117]
	v_pk_mul_f32 v[148:149], v[114:115], v[114:115]
	v_bitop3_b32 v152, v199, s73, 16 bitop3:0xc8
	v_mov_b32_e32 v150, v146
	v_mov_b32_e32 v151, v148
	v_mov_b32_e32 v148, v147
	v_pk_add_f32 v[146:147], v[150:151], v[148:149]
	v_lshlrev_b32_e32 v170, 7, v152
	v_add_f32_e32 v147, v153, v147
	v_lshl_add_u64 v[158:159], v[172:173], 0, v[170:171]
	v_lshl_add_u64 v[150:151], v[174:175], 0, v[170:171]
	v_add_f32_e32 v210, v146, v147
	global_load_dwordx4 v[146:149], v[150:151], off offset:16
	s_nop 0
	global_load_dwordx4 v[150:153], v[150:151], off
	s_nop 0
	global_load_dwordx4 v[154:157], v[158:159], off offset:16
	s_nop 0
	global_load_dwordx4 v[158:161], v[158:159], off
	v_mov_b32_e32 v208, v204
	v_mov_b32_e32 v209, v206
	v_mov_b32_e32 v206, v205
	v_pk_add_f32 v[204:205], v[208:209], v[206:207]
	v_pk_mul_f32 v[206:207], v[90:91], v[90:91]
	v_add_f32_e32 v170, v210, v205
	v_add_f32_e32 v170, v204, v170
	v_pk_mul_f32 v[204:205], v[92:93], v[92:93]
	v_mov_b32_e32 v209, v206
	v_mov_b32_e32 v208, v204
	v_mov_b32_e32 v206, v205
	v_pk_add_f32 v[204:205], v[208:209], v[206:207]
	s_nop 0
	v_add_f32_e32 v170, v205, v170
	v_add_f32_e32 v170, v204, v170
	ds_bpermute_b32 v204, v201, v170
	s_waitcnt lgkmcnt(0)
	v_add_f32_e32 v170, v170, v204
	ds_bpermute_b32 v204, v202, v170
	s_waitcnt lgkmcnt(0)
	v_add_f32_e32 v170, v170, v204
	v_fmamk_f32 v170, v170, 0x3c800000, v195
	v_rsq_f32_e32 v244, v170
	s_nop 0
	v_mul_f32_e32 v245, v170, v244
	v_fma_f32 v245, -v245, v244, 1.0
	v_mul_f32_e32 v246, 0.5, v244
	v_fmac_f32_e32 v244, v245, v246
	v_mul_f32_e32 v170, v200, v244
	s_mov_b64 s[8:9], -1
	v_pk_mul_f32 v[216:217], v[90:91], v[170:171] op_sel_hi:[1,0]
	v_pk_mul_f32 v[210:211], v[114:115], v[170:171] op_sel_hi:[1,0]
	v_pk_mul_f32 v[216:217], v[130:131], v[216:217]
	v_pk_mul_f32 v[210:211], v[138:139], v[210:211]
	v_pk_mul_f32 v[212:213], v[94:95], v[170:171] op_sel_hi:[1,0]
	v_pk_mul_f32 v[214:215], v[96:97], v[170:171] op_sel_hi:[1,0]
	s_waitcnt vmcnt(3)
	v_pk_mul_f32 v[224:225], v[146:147], v[216:217]
	v_pk_mul_f32 v[218:219], v[92:93], v[170:171] op_sel_hi:[1,0]
	s_waitcnt vmcnt(1)
	v_pk_fma_f32 v[224:225], v[154:155], v[210:211], v[224:225] neg_lo:[0,0,1] neg_hi:[0,0,1]
	v_pk_mul_f32 v[154:155], v[154:155], v[216:217]
	v_pk_mul_f32 v[204:205], v[120:121], v[170:171] op_sel_hi:[1,0]
	v_pk_fma_f32 v[154:155], v[146:147], v[210:211], v[154:155]
	v_lshlrev_b32_e32 v146, 3, v229
	v_pk_mul_f32 v[206:207], v[118:119], v[170:171] op_sel_hi:[1,0]
	v_pk_mul_f32 v[208:209], v[116:117], v[170:171] op_sel_hi:[1,0]
	v_pk_mul_f32 v[214:215], v[136:137], v[214:215]
	v_pk_mul_f32 v[212:213], v[134:135], v[212:213]
	v_pk_mul_f32 v[218:219], v[132:133], v[218:219]
	v_and_b32_e32 v146, 0xf8, v146
	v_pk_mul_f32 v[206:207], v[142:143], v[206:207]
	v_pk_mul_f32 v[204:205], v[144:145], v[204:205]
	v_pk_mul_f32 v[208:209], v[140:141], v[208:209]
	v_pk_mul_f32 v[220:221], v[150:151], v[212:213]
	v_pk_mul_f32 v[222:223], v[152:153], v[214:215]
	v_pk_mul_f32 v[226:227], v[148:149], v[218:219]
	v_or3_b32 v146, v228, v146, v184
	s_waitcnt vmcnt(0)
	v_pk_fma_f32 v[222:223], v[160:161], v[204:205], v[222:223] neg_lo:[0,0,1] neg_hi:[0,0,1]
	v_pk_fma_f32 v[220:221], v[158:159], v[206:207], v[220:221] neg_lo:[0,0,1] neg_hi:[0,0,1]
	v_pk_fma_f32 v[226:227], v[156:157], v[208:209], v[226:227] neg_lo:[0,0,1] neg_hi:[0,0,1]
	v_pk_mul_f32 v[158:159], v[158:159], v[212:213]
	v_pk_mul_f32 v[160:161], v[160:161], v[214:215]
	v_pk_mul_f32 v[156:157], v[156:157], v[218:219]
	v_ashrrev_i32_e32 v147, 31, v146
	v_pk_fma_f32 v[152:153], v[152:153], v[204:205], v[160:161]
	v_pk_fma_f32 v[150:151], v[150:151], v[206:207], v[158:159]
	v_pk_fma_f32 v[156:157], v[148:149], v[208:209], v[156:157]
	v_lshl_add_u64 v[158:159], v[146:147], 1, s[54:55]
	v_cvt_pk_f16_f32 v146, v220, v221
	v_cvt_pk_f16_f32 v147, v222, v223
	v_cvt_pk_f16_f32 v148, v224, v225
	v_cvt_pk_f16_f32 v149, v226, v227
	v_bitop3_b32 v184, v199, s74, 32 bitop3:0xc8
	v_cvt_pk_f16_f32 v150, v150, v151
	v_cvt_pk_f16_f32 v151, v152, v153
	v_cvt_pk_f16_f32 v152, v154, v155
	v_cvt_pk_f16_f32 v153, v156, v157
	global_store_dwordx4 v[158:159], v[146:149], off sc1
	v_lshlrev_b32_e32 v170, 7, v184
	v_mul_f32_e32 v204, v105, v105
	v_lshl_add_u64 v[146:147], v[158:159], 0, s[10:11]
	global_store_dwordx4 v[146:147], v[150:153], off sc1
	v_lshl_add_u64 v[158:159], v[174:175], 0, v[170:171]
	v_fmac_f32_e32 v204, v104, v104
	v_lshl_add_u64 v[150:151], v[172:173], 0, v[170:171]
	global_load_dwordx4 v[146:149], v[150:151], off offset:16
	global_load_dwordx4 v[154:157], v[150:151], off
	s_nop 0
	global_load_dwordx4 v[150:153], v[158:159], off offset:16
	s_nop 0
	global_load_dwordx4 v[158:161], v[158:159], off
	v_mul_f32_e32 v170, v103, v103
	v_fmac_f32_e32 v170, v102, v102
	v_add_f32_e32 v170, v170, v204
	v_pk_mul_f32 v[204:205], v[100:101], v[100:101]
	v_pk_mul_f32 v[206:207], v[98:99], v[98:99]
	v_mov_b32_e32 v208, v204
	v_mov_b32_e32 v209, v206
	v_mov_b32_e32 v206, v205
	v_pk_add_f32 v[204:205], v[208:209], v[206:207]
	v_pk_mul_f32 v[206:207], v[78:79], v[78:79]
	v_add_f32_e32 v170, v170, v205
	v_add_f32_e32 v170, v204, v170
	v_pk_mul_f32 v[204:205], v[80:81], v[80:81]
	v_mov_b32_e32 v209, v206
	v_mov_b32_e32 v208, v204
	v_mov_b32_e32 v206, v205
	v_pk_add_f32 v[204:205], v[208:209], v[206:207]
	v_pk_mul_f32 v[206:207], v[74:75], v[74:75]
	v_add_f32_e32 v170, v170, v205
	v_add_f32_e32 v170, v204, v170
	v_pk_mul_f32 v[204:205], v[76:77], v[76:77]
	v_mov_b32_e32 v209, v206
	v_mov_b32_e32 v208, v204
	v_mov_b32_e32 v206, v205
	v_pk_add_f32 v[204:205], v[208:209], v[206:207]
	s_mov_b64 vcc, s[4:5]
	v_add_f32_e32 v170, v205, v170
	v_add_f32_e32 v170, v204, v170
	ds_bpermute_b32 v204, v201, v170
	v_lshlrev_b32_e32 v205, 6, v184
	s_waitcnt lgkmcnt(0)
	v_add_f32_e32 v170, v170, v204
	ds_bpermute_b32 v204, v202, v170
	s_cbranch_vccnz .LBB1_17
	v_or_b32_e32 v184, 32, v199
	v_lshlrev_b32_e32 v184, 3, v184
	v_and_b32_e32 v206, 0x1f000, v205
	v_and_b32_e32 v184, 0x178, v184
	v_or3_b32 v184, v206, v184, v203
	s_mov_b64 s[8:9], 0

.LBB1_20:
	s_waitcnt lgkmcnt(0)
	v_add_f32_e32 v170, v170, v204
	v_fmamk_f32 v170, v170, 0x3c800000, v195
	v_rsq_f32_e32 v244, v170
	s_nop 0
	v_mul_f32_e32 v245, v170, v244
	v_fma_f32 v245, -v245, v244, 1.0
	v_mul_f32_e32 v246, 0.5, v244
	v_fmac_f32_e32 v244, v245, v246
	v_mul_f32_e32 v170, v200, v244
	s_lshl_b32 s10, s56, 1
	v_add_u32_e32 v228, 0x80, v199
	v_pk_mul_f32 v[212:213], v[78:79], v[170:171] op_sel_hi:[1,0]
	v_pk_mul_f32 v[214:215], v[80:81], v[170:171] op_sel_hi:[1,0]
	v_pk_mul_f32 v[216:217], v[74:75], v[170:171] op_sel_hi:[1,0]
	v_pk_mul_f32 v[218:219], v[76:77], v[170:171] op_sel_hi:[1,0]
	v_pk_mul_f32 v[204:205], v[104:105], v[170:171] op_sel_hi:[1,0]
	v_pk_mul_f32 v[206:207], v[102:103], v[170:171] op_sel_hi:[1,0]
	v_pk_mul_f32 v[208:209], v[100:101], v[170:171] op_sel_hi:[1,0]
	v_pk_mul_f32 v[210:211], v[98:99], v[170:171] op_sel_hi:[1,0]
	v_pk_mul_f32 v[214:215], v[136:137], v[214:215]
	v_pk_mul_f32 v[212:213], v[134:135], v[212:213]
	v_pk_mul_f32 v[218:219], v[132:133], v[218:219]
	v_pk_mul_f32 v[216:217], v[130:131], v[216:217]
	v_pk_mul_f32 v[206:207], v[142:143], v[206:207]
	v_pk_mul_f32 v[204:205], v[144:145], v[204:205]
	v_pk_mul_f32 v[210:211], v[138:139], v[210:211]
	v_pk_mul_f32 v[208:209], v[140:141], v[208:209]
	s_waitcnt vmcnt(0)
	v_pk_mul_f32 v[220:221], v[158:159], v[212:213]
	v_pk_mul_f32 v[222:223], v[160:161], v[214:215]
	v_pk_mul_f32 v[224:225], v[150:151], v[216:217]
	v_pk_mul_f32 v[226:227], v[152:153], v[218:219]
	v_pk_fma_f32 v[222:223], v[156:157], v[204:205], v[222:223] neg_lo:[0,0,1] neg_hi:[0,0,1]
	v_pk_fma_f32 v[220:221], v[154:155], v[206:207], v[220:221] neg_lo:[0,0,1] neg_hi:[0,0,1]
	v_pk_fma_f32 v[226:227], v[148:149], v[208:209], v[226:227] neg_lo:[0,0,1] neg_hi:[0,0,1]
	v_pk_fma_f32 v[224:225], v[146:147], v[210:211], v[224:225] neg_lo:[0,0,1] neg_hi:[0,0,1]
	v_pk_mul_f32 v[154:155], v[154:155], v[212:213]
	v_pk_mul_f32 v[156:157], v[156:157], v[214:215]
	v_pk_mul_f32 v[146:147], v[146:147], v[216:217]
	v_pk_mul_f32 v[148:149], v[148:149], v[218:219]
	v_ashrrev_i32_e32 v185, 31, v184
	v_pk_fma_f32 v[156:157], v[160:161], v[204:205], v[156:157]
	v_pk_fma_f32 v[154:155], v[158:159], v[206:207], v[154:155]
	v_pk_fma_f32 v[158:159], v[152:153], v[208:209], v[148:149]
	v_pk_fma_f32 v[152:153], v[150:151], v[210:211], v[146:147]
	v_lshl_add_u64 v[160:161], v[184:185], 1, s[8:9]
	v_cvt_pk_f16_f32 v146, v220, v221
	v_cvt_pk_f16_f32 v147, v222, v223
	v_cvt_pk_f16_f32 v148, v224, v225
	v_cvt_pk_f16_f32 v149, v226, v227
	v_cvt_pk_f16_f32 v150, v154, v155
	v_cvt_pk_f16_f32 v151, v156, v157
	v_cvt_pk_f16_f32 v152, v152, v153
	v_cvt_pk_f16_f32 v153, v158, v159
	global_store_dwordx4 v[160:161], v[146:149], off sc1
	v_bitop3_b32 v226, v199, s75, 48 bitop3:0xc8
	v_lshlrev_b32_e32 v170, 7, v226
	v_lshl_add_u64 v[146:147], v[160:161], 0, s[10:11]
	global_store_dwordx4 v[146:147], v[150:153], off sc1
	v_mul_f32_e32 v146, v87, v87
	v_mul_f32_e32 v147, v89, v89
	v_fmac_f32_e32 v146, v86, v86
	v_fmac_f32_e32 v147, v88, v88
	v_add_f32_e32 v152, v146, v147
	v_pk_mul_f32 v[146:147], v[84:85], v[84:85]
	v_pk_mul_f32 v[148:149], v[82:83], v[82:83]
	v_mov_b32_e32 v150, v146
	v_mov_b32_e32 v151, v148
	v_mov_b32_e32 v148, v147
	v_pk_add_f32 v[146:147], v[150:151], v[148:149]
	v_lshl_add_u64 v[158:159], v[172:173], 0, v[170:171]
	v_add_f32_e32 v147, v152, v147
	v_lshl_add_u64 v[150:151], v[174:175], 0, v[170:171]
	v_add_f32_e32 v208, v146, v147
	global_load_dwordx4 v[146:149], v[150:151], off offset:16
	s_nop 0
	global_load_dwordx4 v[150:153], v[150:151], off
	s_nop 0
	global_load_dwordx4 v[154:157], v[158:159], off offset:16
	s_nop 0
	global_load_dwordx4 v[158:161], v[158:159], off
	v_pk_mul_f32 v[184:185], v[72:73], v[72:73]
	v_pk_mul_f32 v[204:205], v[70:71], v[70:71]
	v_mov_b32_e32 v206, v184
	v_mov_b32_e32 v207, v204
	v_mov_b32_e32 v204, v185
	v_pk_add_f32 v[184:185], v[206:207], v[204:205]
	v_pk_mul_f32 v[204:205], v[66:67], v[66:67]
	v_add_f32_e32 v170, v208, v185
	v_add_f32_e32 v170, v184, v170
	v_pk_mul_f32 v[184:185], v[68:69], v[68:69]
	v_mov_b32_e32 v207, v204
	v_mov_b32_e32 v206, v184
	v_mov_b32_e32 v204, v185
	v_pk_add_f32 v[184:185], v[206:207], v[204:205]
	v_or_b32_e32 v227, 48, v199
	v_add_f32_e32 v170, v185, v170
	v_add_f32_e32 v170, v184, v170
	ds_bpermute_b32 v184, v201, v170
	s_waitcnt lgkmcnt(0)
	v_add_f32_e32 v170, v170, v184
	ds_bpermute_b32 v184, v202, v170
	s_waitcnt lgkmcnt(0)
	v_add_f32_e32 v170, v170, v184
	v_fmamk_f32 v170, v170, 0x3c800000, v195
	v_rsq_f32_e32 v244, v170
	s_nop 0
	v_mul_f32_e32 v245, v170, v244
	v_fma_f32 v245, -v245, v244, 1.0
	v_mul_f32_e32 v246, 0.5, v244
	v_fmac_f32_e32 v244, v245, v246
	v_mul_f32_e32 v170, v200, v244
	v_pk_mul_f32 v[214:215], v[66:67], v[170:171] op_sel_hi:[1,0]
	v_pk_mul_f32 v[208:209], v[82:83], v[170:171] op_sel_hi:[1,0]
	v_pk_mul_f32 v[214:215], v[130:131], v[214:215]
	v_pk_mul_f32 v[208:209], v[138:139], v[208:209]
	s_waitcnt vmcnt(3)
	v_pk_mul_f32 v[222:223], v[146:147], v[214:215]
	v_pk_mul_f32 v[210:211], v[70:71], v[170:171] op_sel_hi:[1,0]
	s_waitcnt vmcnt(1)
	v_pk_fma_f32 v[222:223], v[154:155], v[208:209], v[222:223] neg_lo:[0,0,1] neg_hi:[0,0,1]
	v_pk_mul_f32 v[154:155], v[154:155], v[214:215]
	v_pk_mul_f32 v[212:213], v[72:73], v[170:171] op_sel_hi:[1,0]
	v_pk_mul_f32 v[216:217], v[68:69], v[170:171] op_sel_hi:[1,0]
	v_pk_fma_f32 v[154:155], v[146:147], v[208:209], v[154:155]
	v_lshlrev_b32_e32 v146, 6, v226
	v_lshlrev_b32_e32 v147, 3, v227
	v_pk_mul_f32 v[184:185], v[88:89], v[170:171] op_sel_hi:[1,0]
	v_pk_mul_f32 v[204:205], v[86:87], v[170:171] op_sel_hi:[1,0]
	v_pk_mul_f32 v[206:207], v[84:85], v[170:171] op_sel_hi:[1,0]
	v_pk_mul_f32 v[212:213], v[136:137], v[212:213]
	v_pk_mul_f32 v[210:211], v[134:135], v[210:211]
	v_pk_mul_f32 v[216:217], v[132:133], v[216:217]
	v_and_b32_e32 v146, s79, v146
	v_and_b32_e32 v147, s57, v147
	v_pk_mul_f32 v[204:205], v[142:143], v[204:205]
	v_pk_mul_f32 v[184:185], v[144:145], v[184:185]
	v_pk_mul_f32 v[206:207], v[140:141], v[206:207]
	v_pk_mul_f32 v[218:219], v[150:151], v[210:211]
	v_pk_mul_f32 v[220:221], v[152:153], v[212:213]
	v_pk_mul_f32 v[224:225], v[148:149], v[216:217]
	v_or3_b32 v146, v147, v203, v146
	s_waitcnt vmcnt(0)
	v_pk_fma_f32 v[220:221], v[160:161], v[184:185], v[220:221] neg_lo:[0,0,1] neg_hi:[0,0,1]
	v_pk_fma_f32 v[218:219], v[158:159], v[204:205], v[218:219] neg_lo:[0,0,1] neg_hi:[0,0,1]
	v_pk_fma_f32 v[224:225], v[156:157], v[206:207], v[224:225] neg_lo:[0,0,1] neg_hi:[0,0,1]
	v_pk_mul_f32 v[158:159], v[158:159], v[210:211]
	v_pk_mul_f32 v[160:161], v[160:161], v[212:213]
	v_pk_mul_f32 v[156:157], v[156:157], v[216:217]
	v_ashrrev_i32_e32 v147, 31, v146
	v_pk_fma_f32 v[152:153], v[152:153], v[184:185], v[160:161]
	v_pk_fma_f32 v[150:151], v[150:151], v[204:205], v[158:159]
	v_pk_fma_f32 v[156:157], v[148:149], v[206:207], v[156:157]
	v_lshl_add_u64 v[158:159], v[146:147], 1, s[8:9]
	v_cvt_pk_f16_f32 v146, v218, v219
	v_cvt_pk_f16_f32 v147, v220, v221
	v_cvt_pk_f16_f32 v148, v222, v223
	v_cvt_pk_f16_f32 v149, v224, v225
	v_cvt_pk_f16_f32 v150, v150, v151
	v_cvt_pk_f16_f32 v151, v152, v153
	v_cvt_pk_f16_f32 v152, v154, v155
	v_cvt_pk_f16_f32 v153, v156, v157
	global_store_dwordx4 v[158:159], v[146:149], off sc1
	v_pk_mul_f32 v[184:185], v[48:49], v[48:49]
	v_pk_mul_f32 v[204:205], v[46:47], v[46:47]
	v_lshl_add_u64 v[146:147], v[158:159], 0, s[10:11]
	global_store_dwordx4 v[146:147], v[150:153], off sc1
	v_mul_f32_e32 v146, v63, v63
	v_mul_f32_e32 v147, v65, v65
	v_fmac_f32_e32 v146, v62, v62
	v_fmac_f32_e32 v147, v64, v64
	v_add_f32_e32 v153, v146, v147
	v_pk_mul_f32 v[146:147], v[60:61], v[60:61]
	v_pk_mul_f32 v[148:149], v[58:59], v[58:59]
	v_and_b32_e32 v152, 0x7cf, v228
	v_mov_b32_e32 v150, v146
	v_mov_b32_e32 v151, v148
	v_mov_b32_e32 v148, v147
	v_pk_add_f32 v[146:147], v[150:151], v[148:149]
	v_lshlrev_b32_e32 v170, 7, v152
	v_add_f32_e32 v147, v153, v147
	v_lshl_add_u64 v[158:159], v[172:173], 0, v[170:171]
	v_lshl_add_u64 v[150:151], v[174:175], 0, v[170:171]
	v_add_f32_e32 v203, v146, v147
	global_load_dwordx4 v[146:149], v[150:151], off offset:16
	s_nop 0
	global_load_dwordx4 v[150:153], v[150:151], off
	s_nop 0
	global_load_dwordx4 v[154:157], v[158:159], off offset:16
	s_nop 0
	global_load_dwordx4 v[158:161], v[158:159], off
	v_mov_b32_e32 v206, v184
	v_mov_b32_e32 v207, v204
	v_mov_b32_e32 v204, v185
	v_pk_add_f32 v[184:185], v[206:207], v[204:205]
	v_pk_mul_f32 v[204:205], v[42:43], v[42:43]
	v_add_f32_e32 v170, v203, v185
	v_add_f32_e32 v170, v184, v170
	v_pk_mul_f32 v[184:185], v[44:45], v[44:45]
	v_mov_b32_e32 v207, v204
	v_mov_b32_e32 v206, v184
	v_mov_b32_e32 v204, v185
	v_pk_add_f32 v[184:185], v[206:207], v[204:205]
	s_nop 0
	v_add_f32_e32 v170, v185, v170
	v_add_f32_e32 v170, v184, v170
	ds_bpermute_b32 v184, v201, v170
	v_lshrrev_b32_e32 v185, 8, v228
	v_and_b32_e32 v185, 0x7ff8, v185
	v_add_u32_e32 v185, s78, v185
	v_lshl_or_b32 v203, v185, 17, v187
	s_waitcnt lgkmcnt(0)
	v_add_f32_e32 v170, v170, v184
	ds_bpermute_b32 v184, v202, v170
	v_lshrrev_b32_e32 v185, 6, v228
	v_and_b32_e32 v185, 0x7fe0, v185
	v_add_u32_e32 v185, s37, v185
	v_lshl_or_b32 v185, v185, 17, v188
	s_waitcnt lgkmcnt(0)
	v_add_f32_e32 v170, v170, v184
	v_fmamk_f32 v170, v170, 0x3c800000, v195
	v_rsq_f32_e32 v244, v170
	s_nop 0
	v_mul_f32_e32 v245, v170, v244
	v_fma_f32 v245, -v245, v244, 1.0
	v_mul_f32_e32 v246, 0.5, v244
	v_fmac_f32_e32 v244, v245, v246
	v_mul_f32_e32 v170, v200, v244
	v_pk_mul_f32 v[216:217], v[42:43], v[170:171] op_sel_hi:[1,0]
	v_pk_mul_f32 v[210:211], v[58:59], v[170:171] op_sel_hi:[1,0]
	v_pk_mul_f32 v[216:217], v[130:131], v[216:217]
	v_pk_mul_f32 v[210:211], v[138:139], v[210:211]
	v_pk_mul_f32 v[212:213], v[46:47], v[170:171] op_sel_hi:[1,0]
	v_pk_mul_f32 v[214:215], v[48:49], v[170:171] op_sel_hi:[1,0]
	s_waitcnt vmcnt(3)
	v_pk_mul_f32 v[224:225], v[146:147], v[216:217]
	v_pk_mul_f32 v[218:219], v[44:45], v[170:171] op_sel_hi:[1,0]
	s_waitcnt vmcnt(1)
	v_pk_fma_f32 v[224:225], v[154:155], v[210:211], v[224:225] neg_lo:[0,0,1] neg_hi:[0,0,1]
	v_pk_mul_f32 v[154:155], v[154:155], v[216:217]
	v_pk_mul_f32 v[204:205], v[64:65], v[170:171] op_sel_hi:[1,0]
	v_pk_fma_f32 v[154:155], v[146:147], v[210:211], v[154:155]
	v_lshlrev_b32_e32 v146, 6, v228
	v_pk_mul_f32 v[206:207], v[62:63], v[170:171] op_sel_hi:[1,0]
	v_pk_mul_f32 v[208:209], v[60:61], v[170:171] op_sel_hi:[1,0]
	v_pk_mul_f32 v[214:215], v[136:137], v[214:215]
	v_pk_mul_f32 v[212:213], v[134:135], v[212:213]
	v_pk_mul_f32 v[218:219], v[132:133], v[218:219]
	v_cndmask_b32_e64 v184, v203, v185, s[6:7]
	v_and_b32_e32 v146, 0x1f000, v146
	v_pk_mul_f32 v[206:207], v[142:143], v[206:207]
	v_pk_mul_f32 v[204:205], v[144:145], v[204:205]
	v_pk_mul_f32 v[208:209], v[140:141], v[208:209]
	v_pk_mul_f32 v[220:221], v[150:151], v[212:213]
	v_pk_mul_f32 v[222:223], v[152:153], v[214:215]
	v_pk_mul_f32 v[226:227], v[148:149], v[218:219]
	v_or3_b32 v146, v146, v189, v184
	s_waitcnt vmcnt(0)
	v_pk_fma_f32 v[222:223], v[160:161], v[204:205], v[222:223] neg_lo:[0,0,1] neg_hi:[0,0,1]
	v_pk_fma_f32 v[220:221], v[158:159], v[206:207], v[220:221] neg_lo:[0,0,1] neg_hi:[0,0,1]
	v_pk_fma_f32 v[226:227], v[156:157], v[208:209], v[226:227] neg_lo:[0,0,1] neg_hi:[0,0,1]
	v_pk_mul_f32 v[158:159], v[158:159], v[212:213]
	v_pk_mul_f32 v[160:161], v[160:161], v[214:215]
	v_pk_mul_f32 v[156:157], v[156:157], v[218:219]
	v_ashrrev_i32_e32 v147, 31, v146
	v_pk_fma_f32 v[152:153], v[152:153], v[204:205], v[160:161]
	v_pk_fma_f32 v[150:151], v[150:151], v[206:207], v[158:159]
	v_pk_fma_f32 v[156:157], v[148:149], v[208:209], v[156:157]
	v_lshl_add_u64 v[158:159], v[146:147], 1, s[54:55]
	v_cvt_pk_f16_f32 v146, v220, v221
	v_cvt_pk_f16_f32 v147, v222, v223
	v_cvt_pk_f16_f32 v148, v224, v225
	v_cvt_pk_f16_f32 v149, v226, v227
	v_cvt_pk_f16_f32 v150, v150, v151
	v_cvt_pk_f16_f32 v151, v152, v153
	v_cvt_pk_f16_f32 v152, v154, v155
	v_cvt_pk_f16_f32 v153, v156, v157
	global_store_dwordx4 v[158:159], v[146:149], off sc1
	v_add_u32_e32 v228, 0x90, v199
	v_pk_mul_f32 v[204:205], v[32:33], v[32:33]
	v_lshl_add_u64 v[146:147], v[158:159], 0, s[10:11]
	global_store_dwordx4 v[146:147], v[150:153], off sc1
	v_mul_f32_e32 v146, v55, v55
	v_mul_f32_e32 v147, v57, v57
	v_fmac_f32_e32 v146, v54, v54
	v_fmac_f32_e32 v147, v56, v56
	v_add_f32_e32 v153, v146, v147
	v_pk_mul_f32 v[146:147], v[52:53], v[52:53]
	v_pk_mul_f32 v[148:149], v[50:51], v[50:51]
	v_and_b32_e32 v152, 0x7df, v228
	v_mov_b32_e32 v150, v146
	v_mov_b32_e32 v151, v148
	v_mov_b32_e32 v148, v147
	v_pk_add_f32 v[146:147], v[150:151], v[148:149]
	v_lshlrev_b32_e32 v170, 7, v152
	v_add_f32_e32 v147, v153, v147
	v_lshl_add_u64 v[158:159], v[172:173], 0, v[170:171]
	v_lshl_add_u64 v[150:151], v[174:175], 0, v[170:171]
	v_add_f32_e32 v210, v146, v147
	global_load_dwordx4 v[146:149], v[150:151], off offset:16
	s_nop 0
	global_load_dwordx4 v[150:153], v[150:151], off
	s_nop 0
	global_load_dwordx4 v[154:157], v[158:159], off offset:16
	s_nop 0
	global_load_dwordx4 v[158:161], v[158:159], off
	v_pk_mul_f32 v[206:207], v[30:31], v[30:31]
	v_mov_b32_e32 v208, v204
	v_mov_b32_e32 v209, v206
	v_mov_b32_e32 v206, v205
	v_pk_add_f32 v[204:205], v[208:209], v[206:207]
	v_pk_mul_f32 v[206:207], v[26:27], v[26:27]
	v_add_f32_e32 v170, v210, v205
	v_add_f32_e32 v170, v204, v170
	v_pk_mul_f32 v[204:205], v[28:29], v[28:29]
	v_mov_b32_e32 v209, v206
	v_mov_b32_e32 v208, v204
	v_mov_b32_e32 v206, v205
	v_pk_add_f32 v[204:205], v[208:209], v[206:207]
	s_nop 0
	v_add_f32_e32 v170, v205, v170
	v_add_f32_e32 v170, v204, v170
	ds_bpermute_b32 v204, v201, v170
	s_waitcnt lgkmcnt(0)
	v_add_f32_e32 v170, v170, v204
	ds_bpermute_b32 v204, v202, v170
	s_waitcnt lgkmcnt(0)
	v_add_f32_e32 v170, v170, v204
	v_fmamk_f32 v170, v170, 0x3c800000, v195
	v_rsq_f32_e32 v244, v170
	s_nop 0
	v_mul_f32_e32 v245, v170, v244
	v_fma_f32 v245, -v245, v244, 1.0
	v_mul_f32_e32 v246, 0.5, v244
	v_fmac_f32_e32 v244, v245, v246
	v_mul_f32_e32 v170, v200, v244
	s_mov_b64 s[4:5], -1
	v_pk_mul_f32 v[216:217], v[26:27], v[170:171] op_sel_hi:[1,0]
	v_pk_mul_f32 v[210:211], v[50:51], v[170:171] op_sel_hi:[1,0]
	v_pk_mul_f32 v[216:217], v[130:131], v[216:217]
	v_pk_mul_f32 v[210:211], v[138:139], v[210:211]
	v_pk_mul_f32 v[214:215], v[32:33], v[170:171] op_sel_hi:[1,0]
	s_waitcnt vmcnt(3)
	v_pk_mul_f32 v[224:225], v[146:147], v[216:217]
	v_pk_mul_f32 v[204:205], v[56:57], v[170:171] op_sel_hi:[1,0]
	s_waitcnt vmcnt(1)
	v_pk_fma_f32 v[224:225], v[154:155], v[210:211], v[224:225] neg_lo:[0,0,1] neg_hi:[0,0,1]
	v_pk_mul_f32 v[154:155], v[154:155], v[216:217]
	v_pk_mul_f32 v[212:213], v[30:31], v[170:171] op_sel_hi:[1,0]
	v_pk_mul_f32 v[214:215], v[136:137], v[214:215]
	v_pk_mul_f32 v[218:219], v[28:29], v[170:171] op_sel_hi:[1,0]
	v_pk_fma_f32 v[154:155], v[146:147], v[210:211], v[154:155]
	v_lshlrev_b32_e32 v146, 6, v228
	v_lshlrev_b32_e32 v147, 3, v228
	v_pk_mul_f32 v[206:207], v[54:55], v[170:171] op_sel_hi:[1,0]
	v_pk_mul_f32 v[204:205], v[144:145], v[204:205]
	v_pk_mul_f32 v[208:209], v[52:53], v[170:171] op_sel_hi:[1,0]
	v_pk_mul_f32 v[212:213], v[134:135], v[212:213]
	v_pk_mul_f32 v[218:219], v[132:133], v[218:219]
	v_pk_mul_f32 v[222:223], v[152:153], v[214:215]
	v_and_b32_e32 v146, 0x1f000, v146
	v_and_b32_e32 v147, 0xf8, v147
	v_pk_mul_f32 v[206:207], v[142:143], v[206:207]
	v_pk_mul_f32 v[208:209], v[140:141], v[208:209]
	v_pk_mul_f32 v[220:221], v[150:151], v[212:213]
	s_waitcnt vmcnt(0)
	v_pk_fma_f32 v[222:223], v[160:161], v[204:205], v[222:223] neg_lo:[0,0,1] neg_hi:[0,0,1]
	v_pk_mul_f32 v[226:227], v[148:149], v[218:219]
	v_pk_mul_f32 v[160:161], v[160:161], v[214:215]
	v_or3_b32 v146, v146, v147, v184
	v_pk_fma_f32 v[220:221], v[158:159], v[206:207], v[220:221] neg_lo:[0,0,1] neg_hi:[0,0,1]
	v_pk_fma_f32 v[226:227], v[156:157], v[208:209], v[226:227] neg_lo:[0,0,1] neg_hi:[0,0,1]
	v_pk_mul_f32 v[158:159], v[158:159], v[212:213]
	v_pk_fma_f32 v[152:153], v[152:153], v[204:205], v[160:161]
	v_pk_mul_f32 v[156:157], v[156:157], v[218:219]
	v_ashrrev_i32_e32 v147, 31, v146
	v_add_u32_e32 v204, 0xa0, v199
	v_pk_fma_f32 v[150:151], v[150:151], v[206:207], v[158:159]
	v_pk_fma_f32 v[156:157], v[148:149], v[208:209], v[156:157]
	v_lshl_add_u64 v[158:159], v[146:147], 1, s[54:55]
	v_cvt_pk_f16_f32 v146, v220, v221
	v_cvt_pk_f16_f32 v147, v222, v223
	v_cvt_pk_f16_f32 v148, v224, v225
	v_cvt_pk_f16_f32 v149, v226, v227
	v_and_b32_e32 v184, 0x7ef, v204
	v_cvt_pk_f16_f32 v150, v150, v151
	v_cvt_pk_f16_f32 v151, v152, v153
	v_cvt_pk_f16_f32 v152, v154, v155
	v_cvt_pk_f16_f32 v153, v156, v157
	global_store_dwordx4 v[158:159], v[146:149], off sc1
	v_lshlrev_b32_e32 v170, 7, v184
	v_mul_f32_e32 v205, v41, v41
	v_lshl_add_u64 v[146:147], v[158:159], 0, s[10:11]
	global_store_dwordx4 v[146:147], v[150:153], off sc1
	v_lshl_add_u64 v[158:159], v[174:175], 0, v[170:171]
	v_pk_mul_f32 v[206:207], v[36:37], v[36:37]
	v_lshl_add_u64 v[150:151], v[172:173], 0, v[170:171]
	global_load_dwordx4 v[146:149], v[150:151], off offset:16
	global_load_dwordx4 v[154:157], v[150:151], off
	s_nop 0
	global_load_dwordx4 v[150:153], v[158:159], off offset:16
	s_nop 0
	global_load_dwordx4 v[158:161], v[158:159], off
	v_mul_f32_e32 v170, v39, v39
	v_pk_mul_f32 v[208:209], v[34:35], v[34:35]
	v_fmac_f32_e32 v170, v38, v38
	v_fmac_f32_e32 v205, v40, v40
	v_mov_b32_e32 v210, v206
	v_mov_b32_e32 v211, v208
	v_mov_b32_e32 v208, v207
	v_add_f32_e32 v170, v170, v205
	v_pk_add_f32 v[206:207], v[210:211], v[208:209]
	v_pk_mul_f32 v[208:209], v[14:15], v[14:15]
	v_add_f32_e32 v170, v170, v207
	v_add_f32_e32 v170, v206, v170
	v_pk_mul_f32 v[206:207], v[16:17], v[16:17]
	v_mov_b32_e32 v211, v208
	v_mov_b32_e32 v210, v206
	v_mov_b32_e32 v208, v207
	v_pk_add_f32 v[206:207], v[210:211], v[208:209]
	v_pk_mul_f32 v[208:209], v[10:11], v[10:11]
	v_add_f32_e32 v170, v170, v207
	v_add_f32_e32 v170, v206, v170
	v_pk_mul_f32 v[206:207], v[12:13], v[12:13]
	v_mov_b32_e32 v211, v208
	v_mov_b32_e32 v210, v206
	v_mov_b32_e32 v208, v207
	v_pk_add_f32 v[206:207], v[210:211], v[208:209]
	s_andn2_b64 vcc, exec, s[52:53]
	v_add_f32_e32 v170, v207, v170
	v_add_f32_e32 v170, v206, v170
	ds_bpermute_b32 v205, v201, v170
	v_lshlrev_b32_e32 v206, 6, v184
	s_waitcnt lgkmcnt(0)
	v_add_f32_e32 v170, v170, v205
	ds_bpermute_b32 v205, v202, v170
	s_cbranch_vccnz .LBB1_22
	v_lshlrev_b32_e32 v204, 3, v204
	v_and_b32_e32 v184, 0x1f000, v206
	v_and_b32_e32 v204, 0x178, v204
	v_or3_b32 v184, v184, v204, v203
	s_mov_b64 s[4:5], 0

.LBB1_25:
	s_waitcnt lgkmcnt(0)
	v_add_f32_e32 v170, v170, v205
	v_fmamk_f32 v170, v170, 0x3c800000, v195
	v_rsq_f32_e32 v244, v170
	s_nop 0
	v_mul_f32_e32 v245, v170, v244
	v_fma_f32 v245, -v245, v244, 1.0
	v_mul_f32_e32 v246, 0.5, v244
	v_fmac_f32_e32 v244, v245, v246
	v_mul_f32_e32 v170, v200, v244
	s_lshl_b32 s10, s8, 1
	v_pk_mul_f32 v[212:213], v[14:15], v[170:171] op_sel_hi:[1,0]
	v_pk_mul_f32 v[214:215], v[16:17], v[170:171] op_sel_hi:[1,0]
	v_pk_mul_f32 v[216:217], v[10:11], v[170:171] op_sel_hi:[1,0]
	v_pk_mul_f32 v[218:219], v[12:13], v[170:171] op_sel_hi:[1,0]
	v_pk_mul_f32 v[204:205], v[40:41], v[170:171] op_sel_hi:[1,0]
	v_pk_mul_f32 v[206:207], v[38:39], v[170:171] op_sel_hi:[1,0]
	v_pk_mul_f32 v[208:209], v[36:37], v[170:171] op_sel_hi:[1,0]
	v_pk_mul_f32 v[210:211], v[34:35], v[170:171] op_sel_hi:[1,0]
	v_pk_mul_f32 v[214:215], v[136:137], v[214:215]
	v_pk_mul_f32 v[212:213], v[134:135], v[212:213]
	v_pk_mul_f32 v[218:219], v[132:133], v[218:219]
	v_pk_mul_f32 v[216:217], v[130:131], v[216:217]
	v_pk_mul_f32 v[206:207], v[142:143], v[206:207]
	v_pk_mul_f32 v[204:205], v[144:145], v[204:205]
	v_pk_mul_f32 v[210:211], v[138:139], v[210:211]
	v_pk_mul_f32 v[208:209], v[140:141], v[208:209]
	s_waitcnt vmcnt(0)
	v_pk_mul_f32 v[220:221], v[158:159], v[212:213]
	v_pk_mul_f32 v[222:223], v[160:161], v[214:215]
	v_pk_mul_f32 v[224:225], v[150:151], v[216:217]
	v_pk_mul_f32 v[226:227], v[152:153], v[218:219]
	v_pk_fma_f32 v[222:223], v[156:157], v[204:205], v[222:223] neg_lo:[0,0,1] neg_hi:[0,0,1]
	v_pk_fma_f32 v[220:221], v[154:155], v[206:207], v[220:221] neg_lo:[0,0,1] neg_hi:[0,0,1]
	v_pk_fma_f32 v[226:227], v[148:149], v[208:209], v[226:227] neg_lo:[0,0,1] neg_hi:[0,0,1]
	v_pk_fma_f32 v[224:225], v[146:147], v[210:211], v[224:225] neg_lo:[0,0,1] neg_hi:[0,0,1]
	v_pk_mul_f32 v[154:155], v[154:155], v[212:213]
	v_pk_mul_f32 v[156:157], v[156:157], v[214:215]
	v_pk_mul_f32 v[146:147], v[146:147], v[216:217]
	v_pk_mul_f32 v[148:149], v[148:149], v[218:219]
	v_ashrrev_i32_e32 v185, 31, v184
	v_pk_fma_f32 v[156:157], v[160:161], v[204:205], v[156:157]
	v_pk_fma_f32 v[154:155], v[158:159], v[206:207], v[154:155]
	v_pk_fma_f32 v[158:159], v[152:153], v[208:209], v[148:149]
	v_pk_fma_f32 v[152:153], v[150:151], v[210:211], v[146:147]
	v_lshl_add_u64 v[160:161], v[184:185], 1, s[6:7]
	v_cvt_pk_f16_f32 v146, v220, v221
	v_cvt_pk_f16_f32 v147, v222, v223
	v_cvt_pk_f16_f32 v148, v224, v225
	v_cvt_pk_f16_f32 v149, v226, v227
	v_cvt_pk_f16_f32 v150, v154, v155
	v_cvt_pk_f16_f32 v151, v156, v157
	v_cvt_pk_f16_f32 v152, v152, v153
	v_cvt_pk_f16_f32 v153, v158, v159
	global_store_dwordx4 v[160:161], v[146:149], off sc1
	v_add_u32_e32 v208, 0xb0, v199
	v_and_b32_e32 v209, 0x7ff, v208
	v_lshl_add_u64 v[146:147], v[160:161], 0, s[10:11]
	global_store_dwordx4 v[146:147], v[150:153], off sc1
	v_mul_f32_e32 v146, v23, v23
	v_mul_f32_e32 v147, v25, v25
	v_fmac_f32_e32 v146, v22, v22
	v_fmac_f32_e32 v147, v24, v24
	v_add_f32_e32 v152, v146, v147
	v_pk_mul_f32 v[146:147], v[20:21], v[20:21]
	v_pk_mul_f32 v[148:149], v[18:19], v[18:19]
	v_mov_b32_e32 v150, v146
	v_mov_b32_e32 v151, v148
	v_mov_b32_e32 v148, v147
	v_pk_add_f32 v[146:147], v[150:151], v[148:149]
	v_lshlrev_b32_e32 v170, 7, v209
	v_add_f32_e32 v147, v152, v147
	v_lshl_add_u64 v[158:159], v[172:173], 0, v[170:171]
	v_lshl_add_u64 v[150:151], v[174:175], 0, v[170:171]
	v_add_f32_e32 v210, v146, v147
	global_load_dwordx4 v[146:149], v[150:151], off offset:16
	s_nop 0
	global_load_dwordx4 v[150:153], v[150:151], off
	s_nop 0
	global_load_dwordx4 v[154:157], v[158:159], off offset:16
	s_nop 0
	global_load_dwordx4 v[158:161], v[158:159], off
	v_pk_mul_f32 v[184:185], v[8:9], v[8:9]
	v_pk_mul_f32 v[204:205], v[6:7], v[6:7]
	v_mov_b32_e32 v206, v184
	v_mov_b32_e32 v207, v204
	v_mov_b32_e32 v204, v185
	v_pk_add_f32 v[184:185], v[206:207], v[204:205]
	v_pk_mul_f32 v[204:205], v[2:3], v[2:3]
	v_add_f32_e32 v170, v210, v185
	v_add_f32_e32 v170, v184, v170
	v_pk_mul_f32 v[184:185], v[4:5], v[4:5]
	v_mov_b32_e32 v207, v204
	v_mov_b32_e32 v206, v184
	v_mov_b32_e32 v204, v185
	v_pk_add_f32 v[184:185], v[206:207], v[204:205]
	s_nop 0
	v_add_f32_e32 v170, v185, v170
	v_add_f32_e32 v170, v184, v170
	ds_bpermute_b32 v184, v201, v170
	s_waitcnt lgkmcnt(0)
	v_add_f32_e32 v170, v170, v184
	ds_bpermute_b32 v184, v202, v170
	s_waitcnt lgkmcnt(0)
	v_add_f32_e32 v170, v170, v184
	v_fmamk_f32 v170, v170, 0x3c800000, v195
	v_rsq_f32_e32 v244, v170
	s_nop 0
	v_mul_f32_e32 v245, v170, v244
	v_fma_f32 v245, -v245, v244, 1.0
	v_mul_f32_e32 v246, 0.5, v244
	v_fmac_f32_e32 v244, v245, v246
	v_mul_f32_e32 v170, v200, v244
	v_pk_mul_f32 v[184:185], v[24:25], v[170:171] op_sel_hi:[1,0]
	v_pk_mul_f32 v[200:201], v[22:23], v[170:171] op_sel_hi:[1,0]
	v_pk_mul_f32 v[144:145], v[144:145], v[184:185]
	v_pk_mul_f32 v[184:185], v[20:21], v[170:171] op_sel_hi:[1,0]
	v_pk_mul_f32 v[142:143], v[142:143], v[200:201]
	v_pk_mul_f32 v[140:141], v[140:141], v[184:185]
	v_pk_mul_f32 v[184:185], v[6:7], v[170:171] op_sel_hi:[1,0]
	v_pk_mul_f32 v[200:201], v[18:19], v[170:171] op_sel_hi:[1,0]
	v_pk_mul_f32 v[134:135], v[134:135], v[184:185]
	v_pk_mul_f32 v[184:185], v[2:3], v[170:171] op_sel_hi:[1,0]
	v_pk_mul_f32 v[138:139], v[138:139], v[200:201]
	v_pk_mul_f32 v[130:131], v[130:131], v[184:185]
	v_pk_mul_f32 v[200:201], v[8:9], v[170:171] op_sel_hi:[1,0]
	s_waitcnt vmcnt(3)
	v_pk_mul_f32 v[204:205], v[146:147], v[130:131]
	s_waitcnt vmcnt(1)
	v_pk_mul_f32 v[130:131], v[154:155], v[130:131]
	v_pk_mul_f32 v[136:137], v[136:137], v[200:201]
	v_pk_mul_f32 v[200:201], v[4:5], v[170:171] op_sel_hi:[1,0]
	v_pk_fma_f32 v[204:205], v[154:155], v[138:139], v[204:205] neg_lo:[0,0,1] neg_hi:[0,0,1]
	v_pk_fma_f32 v[138:139], v[146:147], v[138:139], v[130:131]
	v_lshlrev_b32_e32 v130, 6, v209
	v_lshlrev_b32_e32 v131, 3, v208
	v_pk_mul_f32 v[132:133], v[132:133], v[200:201]
	v_and_b32_e32 v130, s37, v130
	v_and_b32_e32 v131, s9, v131
	v_pk_mul_f32 v[184:185], v[150:151], v[134:135]
	v_pk_mul_f32 v[200:201], v[152:153], v[136:137]
	v_pk_mul_f32 v[206:207], v[148:149], v[132:133]
	v_or3_b32 v130, v131, v203, v130
	s_waitcnt vmcnt(0)
	v_pk_fma_f32 v[200:201], v[160:161], v[144:145], v[200:201] neg_lo:[0,0,1] neg_hi:[0,0,1]
	v_pk_fma_f32 v[184:185], v[158:159], v[142:143], v[184:185] neg_lo:[0,0,1] neg_hi:[0,0,1]
	v_pk_fma_f32 v[206:207], v[156:157], v[140:141], v[206:207] neg_lo:[0,0,1] neg_hi:[0,0,1]
	v_pk_mul_f32 v[134:135], v[158:159], v[134:135]
	v_pk_mul_f32 v[136:137], v[160:161], v[136:137]
	v_pk_mul_f32 v[132:133], v[156:157], v[132:133]
	v_ashrrev_i32_e32 v131, 31, v130
	v_pk_fma_f32 v[136:137], v[152:153], v[144:145], v[136:137]
	v_pk_fma_f32 v[134:135], v[150:151], v[142:143], v[134:135]
	v_pk_fma_f32 v[140:141], v[148:149], v[140:141], v[132:133]
	v_lshl_add_u64 v[142:143], v[130:131], 1, s[6:7]
	v_cvt_pk_f16_f32 v130, v184, v185
	v_cvt_pk_f16_f32 v131, v200, v201
	v_cvt_pk_f16_f32 v132, v204, v205
	v_cvt_pk_f16_f32 v133, v206, v207
	v_cvt_pk_f16_f32 v134, v134, v135
	v_cvt_pk_f16_f32 v135, v136, v137
	v_cvt_pk_f16_f32 v136, v138, v139
	v_cvt_pk_f16_f32 v137, v140, v141
	global_store_dwordx4 v[142:143], v[130:133], off sc1
	s_nop 1
	v_lshl_add_u64 v[130:131], v[142:143], 0, s[10:11]
	global_store_dwordx4 v[130:131], v[134:137], off sc1
	s_branch .LBB1_14

	.amdhsa_kernel _Z15gemm_qkv_kernelPKDF16_S0_PDF16_S1_S1_PKfS3_S3_S3_S3_S1_PKiPyPj
		.amdhsa_group_segment_fixed_size 0
		.amdhsa_private_segment_fixed_size 0
		.amdhsa_kernarg_size 112
		.amdhsa_user_sgpr_count 2
		.amdhsa_user_sgpr_dispatch_ptr 0
		.amdhsa_user_sgpr_queue_ptr 0
		.amdhsa_user_sgpr_kernarg_segment_ptr 1
		.amdhsa_user_sgpr_dispatch_id 0
		.amdhsa_user_sgpr_kernarg_preload_length 0
		.amdhsa_user_sgpr_kernarg_preload_offset 0
		.amdhsa_user_sgpr_private_segment_size 0
		.amdhsa_uses_dynamic_stack 0
		.amdhsa_enable_private_segment 0
		.amdhsa_system_sgpr_workgroup_id_x 1
		.amdhsa_system_sgpr_workgroup_id_y 0
		.amdhsa_system_sgpr_workgroup_id_z 0
		.amdhsa_system_sgpr_workgroup_info 0
		.amdhsa_system_vgpr_workitem_id 0
		.amdhsa_next_free_vgpr 248
		.amdhsa_next_free_sgpr 84
		.amdhsa_accum_offset 248
		.amdhsa_reserve_vcc 1
		.amdhsa_float_round_mode_32 0
		.amdhsa_float_round_mode_16_64 0
		.amdhsa_float_denorm_mode_32 3
		.amdhsa_float_denorm_mode_16_64 3
		.amdhsa_dx10_clamp 1
		.amdhsa_ieee_mode 1
		.amdhsa_fp16_overflow 0
		.amdhsa_tg_split 0
		.amdhsa_exception_fp_ieee_invalid_op 0
		.amdhsa_exception_fp_denorm_src 0
		.amdhsa_exception_fp_ieee_div_zero 0
		.amdhsa_exception_fp_ieee_overflow 0
		.amdhsa_exception_fp_ieee_underflow 0
		.amdhsa_exception_fp_ieee_inexact 0
		.amdhsa_exception_int_div_zero 0
	.end_amdhsa_kernel

amdhsa.kernels:
  - .agpr_count:     0
    .args:
      - .actual_access:  read_only
        .address_space:  global
        .offset:         0
        .size:           8
        .value_kind:     global_buffer
      - .actual_access:  read_only
        .address_space:  global
        .offset:         8
        .size:           8
        .value_kind:     global_buffer
      - .actual_access:  read_only
        .address_space:  global
        .offset:         16
        .size:           8
        .value_kind:     global_buffer
      - .actual_access:  write_only
        .address_space:  global
        .offset:         24
        .size:           8
        .value_kind:     global_buffer
      - .actual_access:  write_only
        .address_space:  global
        .offset:         32
        .size:           8
        .value_kind:     global_buffer
      - .actual_access:  write_only
        .address_space:  global
        .offset:         40
        .size:           8
        .value_kind:     global_buffer
      - .actual_access:  write_only
        .address_space:  global
        .offset:         48
        .size:           8
        .value_kind:     global_buffer
    .group_segment_fixed_size: 0
    .kernarg_segment_align: 8
    .kernarg_segment_size: 56
    .language:       OpenCL C
    .language_version:
      - 2
      - 0
    .max_flat_workgroup_size: 1024
    .name:           _Z11prep_kernelPKfS0_PKiPDF16_S3_PfS4_
    .private_segment_fixed_size: 0
    .sgpr_count:     24
    .sgpr_spill_count: 0
    .symbol:         _Z11prep_kernelPKfS0_PKiPDF16_S3_PfS4_.kd
    .uniform_work_group_size: 1
    .uses_dynamic_stack: false
    .vgpr_count:     40
    .vgpr_spill_count: 0
    .wavefront_size: 64
  - .agpr_count:     0
    .args:
      - .address_space:  global
        .offset:         0
        .size:           8
        .value_kind:     global_buffer
      - .address_space:  global
        .offset:         8
        .size:           8
        .value_kind:     global_buffer
      - .address_space:  global
        .offset:         16
        .size:           8
        .value_kind:     global_buffer
      - .address_space:  global
        .offset:         24
        .size:           8
        .value_kind:     global_buffer
      - .address_space:  global
        .offset:         32
        .size:           8
        .value_kind:     global_buffer
      - .address_space:  global
        .offset:         40
        .size:           8
        .value_kind:     global_buffer
      - .address_space:  global
        .offset:         48
        .size:           8
        .value_kind:     global_buffer
      - .address_space:  global
        .offset:         56
        .size:           8
        .value_kind:     global_buffer
      - .address_space:  global
        .offset:         64
        .size:           8
        .value_kind:     global_buffer
      - .address_space:  global
        .offset:         72
        .size:           8
        .value_kind:     global_buffer
      - .address_space:  global
        .offset:         80
        .size:           8
        .value_kind:     global_buffer
      - .address_space:  global
        .offset:         88
        .size:           8
        .value_kind:     global_buffer
      - .address_space:  global
        .offset:         96
        .size:           8
        .value_kind:     global_buffer
      - .address_space:  global
        .offset:         104
        .size:           8
        .value_kind:     global_buffer
    .group_segment_fixed_size: 0
    .kernarg_segment_align: 8
    .kernarg_segment_size: 112
    .language:       OpenCL C
    .language_version:
      - 2
      - 0
    .max_flat_workgroup_size: 512
    .name:           _Z15gemm_qkv_kernelPKDF16_S0_PDF16_S1_S1_PKfS3_S3_S3_S3_S1_PKiPyPj
    .private_segment_fixed_size: 0
    .sgpr_count:     90
    .sgpr_spill_count: 0
    .symbol:         _Z15gemm_qkv_kernelPKDF16_S0_PDF16_S1_S1_PKfS3_S3_S3_S3_S1_PKiPyPj.kd
    .uniform_work_group_size: 1
    .uses_dynamic_stack: false
    .vgpr_count:     248
    .vgpr_spill_count: 0
    .wavefront_size: 64
  - .agpr_count:     0
    .args:
      - .address_space:  global
        .offset:         0
        .size:           8
        .value_kind:     global_buffer
      - .address_space:  global
        .offset:         8
        .size:           8
        .value_kind:     global_buffer
      - .address_space:  global
        .offset:         16
        .size:           8
        .value_kind:     global_buffer
    .group_segment_fixed_size: 0
    .kernarg_segment_align: 8
    .kernarg_segment_size: 24
    .language:       OpenCL C
    .language_version:
      - 2
      - 0
    .max_flat_workgroup_size: 512
    .name:           _Z15gemm_out_kernelPKDF16_S0_Pf
    .private_segment_fixed_size: 0
    .sgpr_count:     26
    .sgpr_spill_count: 0
    .symbol:         _Z15gemm_out_kernelPKDF16_S0_Pf.kd
    .uniform_work_group_size: 1
    .uses_dynamic_stack: false
    .vgpr_count:     148
    .vgpr_spill_count: 0
    .wavefront_size: 64
  - .agpr_count:     0
    .args:
      - .address_space:  global
        .offset:         0
        .size:           8
        .value_kind:     global_buffer
      - .address_space:  global
        .offset:         8
        .size:           8
        .value_kind:     global_buffer
      - .address_space:  global
        .offset:         16
        .size:           8
        .value_kind:     global_buffer
      - .address_space:  global
        .offset:         24
        .size:           8
        .value_kind:     global_buffer
      - .address_space:  global
        .offset:         32
        .size:           8
        .value_kind:     global_buffer
      - .address_space:  global
        .offset:         40
        .size:           8
        .value_kind:     global_buffer
    .group_segment_fixed_size: 0
    .kernarg_segment_align: 8
    .kernarg_segment_size: 48
    .language:       OpenCL C
    .language_version:
      - 2
      - 0
    .max_flat_workgroup_size: 512
    .name:           _Z11attn_kernelPKDF16_S0_S0_PDF16_PKjS3_
    .private_segment_fixed_size: 0
    .sgpr_count:     68
    .sgpr_spill_count: 0
    .symbol:         _Z11attn_kernelPKDF16_S0_S0_PDF16_PKjS3_.kd
    .uniform_work_group_size: 1
    .uses_dynamic_stack: false
    .vgpr_count:     248
    .vgpr_spill_count: 0
    .wavefront_size: 64
